# adds: P10 TOPE load of the row block hoisted into the first load batch (no separate round trip before the slot scan)
# speedup vs baseline: 1.0002x; 1.0002x over previous
.LBB0_1153:
	s_lshl_b32 s40, s39, 5
	s_add_i32 s12, s40, s35
	s_ashr_i32 s13, s12, 31
	s_lshl_b64 s[24:25], s[12:13], 2
	s_add_u32 s24, s33, s24
	s_addc_u32 s25, s34, s25
	s_lshl_b64 s[26:27], s[12:13], 12
	v_lshl_add_u64 v[90:91], v[40:41], 0, s[26:27]
	global_load_dwordx2 v[150:151], v[90:91], off
	global_load_dwordx2 v[152:153], v[90:91], off offset:512
	global_load_dwordx2 v[154:155], v[90:91], off offset:1024
	global_load_dwordx4 v[2:5], v39, s[24:25]
	global_load_dwordx4 v[34:37], v[42:43], off
	global_load_dwordx4 v[30:33], v[42:43], off offset:1024
	global_load_dwordx4 v[26:29], v[42:43], off offset:2048
	global_load_dwordx4 v[22:25], v[42:43], off offset:3072
	global_load_dwordx4 v[18:21], v[44:45], off
	global_load_dwordx4 v[14:17], v[46:47], off
	global_load_dwordx4 v[10:13], v[48:49], off
	global_load_dwordx4 v[6:9], v[50:51], off
	global_load_dwordx2 v[156:157], v[90:91], off offset:1536
	global_load_dwordx2 v[158:159], v[90:91], off offset:2048
	global_load_dwordx2 v[160:161], v[90:91], off offset:2560
	global_load_dwordx2 v[162:163], v[90:91], off offset:3072
	global_load_dwordx2 v[164:165], v[90:91], off offset:3584
	s_or_b32 s28, s12, 1
	s_or_b32 s26, s12, 2
	s_or_b32 s24, s12, 3
	s_ashr_i32 s29, s28, 31
	s_ashr_i32 s27, s26, 31
	s_ashr_i32 s25, s24, 31
	s_lshl_b64 s[30:31], s[28:29], 12
	s_lshl_b64 s[42:43], s[26:27], 12
	s_lshl_b64 s[44:45], s[24:25], 12
	v_lshl_add_u64 v[90:91], v[40:41], 0, s[30:31]
	v_lshl_add_u64 v[92:93], v[40:41], 0, s[42:43]
	v_lshl_add_u64 v[166:167], v[40:41], 0, s[44:45]
	global_load_dwordx2 v[168:169], v[90:91], off
	global_load_dwordx2 v[170:171], v[90:91], off offset:512
	global_load_dwordx2 v[172:173], v[90:91], off offset:1024
	global_load_dwordx2 v[174:175], v[90:91], off offset:1536
	global_load_dwordx2 v[128:129], v[90:91], off offset:2048
	global_load_dwordx2 v[126:127], v[90:91], off offset:2560
	global_load_dwordx2 v[124:125], v[90:91], off offset:3072
	global_load_dwordx2 v[122:123], v[90:91], off offset:3584
	global_load_dwordx2 v[120:121], v[92:93], off
	global_load_dwordx2 v[118:119], v[92:93], off offset:512
	global_load_dwordx2 v[116:117], v[92:93], off offset:1024
	global_load_dwordx2 v[114:115], v[92:93], off offset:1536
	global_load_dwordx2 v[112:113], v[92:93], off offset:2048
	global_load_dwordx2 v[110:111], v[92:93], off offset:2560
	global_load_dwordx2 v[108:109], v[92:93], off offset:3072
	global_load_dwordx2 v[106:107], v[92:93], off offset:3584
	global_load_dwordx2 v[104:105], v[166:167], off
	global_load_dwordx2 v[102:103], v[166:167], off offset:512
	global_load_dwordx2 v[100:101], v[166:167], off offset:1024
	global_load_dwordx2 v[98:99], v[166:167], off offset:1536
	global_load_dwordx2 v[96:97], v[166:167], off offset:2048
	global_load_dwordx2 v[94:95], v[166:167], off offset:2560
	global_load_dwordx2 v[92:93], v[166:167], off offset:3072
	global_load_dwordx2 v[90:91], v[166:167], off offset:3584
	global_load_dword v198, v[54:55], off
	global_load_dword v199, v[56:57], off
	global_load_dword v200, v[58:59], off
	global_load_dword v201, v[60:61], off
	global_load_dword v202, v[62:63], off
	global_load_dword v203, v[64:65], off
	global_load_dword v204, v[66:67], off
	global_load_dword v205, v[68:69], off
	global_load_dword v206, v[70:71], off
	global_load_dword v207, v[72:73], off
	global_load_dword v208, v[74:75], off
	global_load_dword v209, v[76:77], off
	global_load_dword v210, v[78:79], off
	global_load_dword v211, v[80:81], off
	global_load_dword v212, v[82:83], off
	global_load_dword v213, v[84:85], off
	v_lshl_or_b32 v214, s39, 7, v0
	v_ashrrev_i32_e32 v215, 31, v214
	v_lshl_add_u64 v[214:215], v[214:215], 2, s[14:15]
	global_load_dword v216, v[214:215], off
	v_mov_b32_e32 v177, 0
	v_mov_b32_e32 v176, 0
	s_lshl_b64 s[12:13], s[12:13], 11
	s_waitcnt vmcnt(0)
	v_lshlrev_b32_e32 v166, 16, v150
	v_lshlrev_b32_e32 v178, 16, v152
	v_and_b32_e32 v152, 0xffff0000, v152
	v_mul_f32_e32 v178, v2, v178
	v_mul_f32_e32 v152, v2, v152
	v_mul_f32_e32 v178, v178, v30
	v_mul_f32_e32 v152, v152, v31
	v_and_b32_e32 v150, 0xffff0000, v150
	v_cvt_pk_fp8_f32 v177, v178, v152
	v_lshlrev_b32_e32 v179, 16, v153
	v_and_b32_e32 v153, 0xffff0000, v153
	v_mul_f32_e32 v166, v2, v166
	v_mul_f32_e32 v150, v2, v150
	v_mul_f32_e32 v179, v2, v179
	v_mul_f32_e32 v153, v2, v153
	v_mul_f32_e32 v166, v166, v34
	v_mul_f32_e32 v150, v150, v35
	v_lshlrev_b32_e32 v180, 16, v154
	v_and_b32_e32 v154, 0xffff0000, v154
	v_mul_f32_e32 v179, v179, v32
	v_cvt_pk_fp8_f32 v176, v166, v150
	v_mul_f32_e32 v150, v153, v33
	v_lshlrev_b32_e32 v167, 16, v151
	v_and_b32_e32 v151, 0xffff0000, v151
	v_mul_f32_e32 v180, v2, v180
	v_cvt_pk_fp8_f32 v177, v179, v150 op_sel:[0,0,1]
	v_mul_f32_e32 v150, v2, v154
	v_mul_f32_e32 v167, v2, v167
	v_mul_f32_e32 v151, v2, v151
	v_mul_f32_e32 v152, v180, v26
	v_mul_f32_e32 v150, v150, v27
	v_mov_b32_e32 v153, 0
	v_mul_f32_e32 v167, v167, v36
	v_mul_f32_e32 v151, v151, v37
	v_cvt_pk_fp8_f32 v153, v152, v150
	v_cvt_pk_fp8_f32 v176, v167, v151 op_sel:[0,0,1]
	v_lshlrev_b32_e32 v151, 16, v155
	v_and_b32_e32 v150, 0xffff0000, v155
	v_mul_f32_e32 v151, v2, v151
	v_mul_f32_e32 v150, v2, v150
	v_mul_f32_e32 v151, v151, v28
	v_mul_f32_e32 v150, v150, v29
	v_cvt_pk_fp8_f32 v153, v151, v150 op_sel:[0,0,1]
	v_lshlrev_b32_e32 v150, 16, v156
	v_and_b32_e32 v151, 0xffff0000, v156
	v_mul_f32_e32 v150, v2, v150
	v_mul_f32_e32 v151, v2, v151
	v_mul_f32_e32 v150, v150, v22
	v_mul_f32_e32 v151, v151, v23
	v_mov_b32_e32 v154, 0
	v_cvt_pk_fp8_f32 v154, v150, v151
	v_lshlrev_b32_e32 v152, 16, v157
	v_and_b32_e32 v150, 0xffff0000, v157
	v_mul_f32_e32 v152, v2, v152
	v_mul_f32_e32 v150, v2, v150
	v_mul_f32_e32 v152, v152, v24
	v_mul_f32_e32 v150, v150, v25
	v_cvt_pk_fp8_f32 v154, v152, v150 op_sel:[0,0,1]
	v_lshlrev_b32_e32 v150, 16, v158
	v_and_b32_e32 v151, 0xffff0000, v158
	v_mul_f32_e32 v150, v2, v150
	v_mul_f32_e32 v151, v2, v151
	v_mul_f32_e32 v150, v150, v18
	v_mul_f32_e32 v151, v151, v19
	v_mov_b32_e32 v155, 0
	v_cvt_pk_fp8_f32 v155, v150, v151
	v_lshlrev_b32_e32 v152, 16, v159
	v_and_b32_e32 v150, 0xffff0000, v159
	v_mul_f32_e32 v152, v2, v152
	v_mul_f32_e32 v150, v2, v150
	v_mul_f32_e32 v152, v152, v20
	v_mul_f32_e32 v150, v150, v21
	v_cvt_pk_fp8_f32 v155, v152, v150 op_sel:[0,0,1]
	v_lshlrev_b32_e32 v150, 16, v160
	v_and_b32_e32 v151, 0xffff0000, v160
	v_mul_f32_e32 v150, v2, v150
	v_mul_f32_e32 v151, v2, v151
	v_mul_f32_e32 v150, v150, v14
	v_mul_f32_e32 v151, v151, v15
	v_mov_b32_e32 v156, 0
	v_cvt_pk_fp8_f32 v156, v150, v151
	v_lshlrev_b32_e32 v152, 16, v161
	v_and_b32_e32 v150, 0xffff0000, v161
	v_mul_f32_e32 v152, v2, v152
	v_mul_f32_e32 v150, v2, v150
	v_mul_f32_e32 v152, v152, v16
	v_mul_f32_e32 v150, v150, v17
	v_cvt_pk_fp8_f32 v156, v152, v150 op_sel:[0,0,1]
	v_lshlrev_b32_e32 v150, 16, v162
	v_and_b32_e32 v151, 0xffff0000, v162
	v_mul_f32_e32 v150, v2, v150
	v_mul_f32_e32 v151, v2, v151
	v_mul_f32_e32 v150, v150, v10
	v_mul_f32_e32 v151, v151, v11
	v_mov_b32_e32 v157, 0
	v_cvt_pk_fp8_f32 v157, v150, v151
	v_lshlrev_b32_e32 v152, 16, v163
	v_and_b32_e32 v150, 0xffff0000, v163
	v_mul_f32_e32 v152, v2, v152
	v_mul_f32_e32 v150, v2, v150
	v_mul_f32_e32 v152, v152, v12
	v_mul_f32_e32 v150, v150, v13
	v_cvt_pk_fp8_f32 v157, v152, v150 op_sel:[0,0,1]
	v_lshlrev_b32_e32 v150, 16, v164
	v_and_b32_e32 v151, 0xffff0000, v164
	v_mul_f32_e32 v150, v2, v150
	v_mul_f32_e32 v151, v2, v151
	v_mul_f32_e32 v150, v150, v6
	v_mul_f32_e32 v151, v151, v7
	v_mov_b32_e32 v158, 0
	v_cvt_pk_fp8_f32 v158, v150, v151
	v_lshlrev_b32_e32 v152, 16, v165
	v_and_b32_e32 v150, 0xffff0000, v165
	v_mul_f32_e32 v152, v2, v152
	v_mul_f32_e32 v2, v2, v150
	v_mul_f32_e32 v152, v152, v8
	v_mul_f32_e32 v2, v2, v9
	v_cvt_pk_fp8_f32 v158, v152, v2 op_sel:[0,0,1]
	v_lshlrev_b32_e32 v2, 16, v168
	v_and_b32_e32 v150, 0xffff0000, v168
	v_mul_f32_e32 v2, v3, v2
	v_mul_f32_e32 v150, v3, v150
	v_mul_f32_e32 v2, v2, v34
	v_mul_f32_e32 v150, v150, v35
	v_mov_b32_e32 v152, 0
	v_cvt_pk_fp8_f32 v152, v2, v150
	v_lshlrev_b32_e32 v151, 16, v169
	v_and_b32_e32 v2, 0xffff0000, v169
	v_mul_f32_e32 v151, v3, v151
	v_mul_f32_e32 v2, v3, v2
	v_mul_f32_e32 v151, v151, v36
	v_mul_f32_e32 v2, v2, v37
	v_cvt_pk_fp8_f32 v152, v151, v2 op_sel:[0,0,1]
	v_lshlrev_b32_e32 v2, 16, v170
	v_and_b32_e32 v150, 0xffff0000, v170
	v_mul_f32_e32 v2, v3, v2
	v_mul_f32_e32 v150, v3, v150
	ds_write2st64_b32 v130, v176, v177 offset0:64 offset1:65
	ds_write2st64_b32 v130, v153, v154 offset0:66 offset1:67
	ds_write2st64_b32 v130, v155, v156 offset0:68 offset1:69
	ds_write2st64_b32 v130, v157, v158 offset0:70 offset1:71
	v_mul_f32_e32 v2, v2, v30
	v_mul_f32_e32 v150, v150, v31
	v_mov_b32_e32 v153, 0
	v_cvt_pk_fp8_f32 v153, v2, v150
	v_lshlrev_b32_e32 v151, 16, v171
	v_and_b32_e32 v2, 0xffff0000, v171
	v_mul_f32_e32 v151, v3, v151
	v_mul_f32_e32 v2, v3, v2
	v_mul_f32_e32 v151, v151, v32
	v_mul_f32_e32 v2, v2, v33
	v_cvt_pk_fp8_f32 v153, v151, v2 op_sel:[0,0,1]
	v_lshlrev_b32_e32 v2, 16, v172
	v_and_b32_e32 v150, 0xffff0000, v172
	v_mul_f32_e32 v2, v3, v2
	v_mul_f32_e32 v150, v3, v150
	v_mul_f32_e32 v2, v2, v26
	v_mul_f32_e32 v150, v150, v27
	v_mov_b32_e32 v154, 0
	v_cvt_pk_fp8_f32 v154, v2, v150
	v_lshlrev_b32_e32 v151, 16, v173
	v_and_b32_e32 v2, 0xffff0000, v173
	v_mul_f32_e32 v151, v3, v151
	v_mul_f32_e32 v2, v3, v2
	v_mul_f32_e32 v151, v151, v28
	v_mul_f32_e32 v2, v2, v29
	v_cvt_pk_fp8_f32 v154, v151, v2 op_sel:[0,0,1]
	v_lshlrev_b32_e32 v2, 16, v174
	v_and_b32_e32 v150, 0xffff0000, v174
	v_mul_f32_e32 v2, v3, v2
	v_mul_f32_e32 v150, v3, v150
	v_mul_f32_e32 v2, v2, v22
	v_mul_f32_e32 v150, v150, v23
	v_mov_b32_e32 v155, 0
	v_cvt_pk_fp8_f32 v155, v2, v150
	v_lshlrev_b32_e32 v151, 16, v175
	v_and_b32_e32 v2, 0xffff0000, v175
	v_mul_f32_e32 v151, v3, v151
	v_mul_f32_e32 v2, v3, v2
	v_mul_f32_e32 v151, v151, v24
	v_mul_f32_e32 v2, v2, v25
	v_cvt_pk_fp8_f32 v155, v151, v2 op_sel:[0,0,1]
	v_lshlrev_b32_e32 v2, 16, v128
	v_and_b32_e32 v128, 0xffff0000, v128
	v_mul_f32_e32 v2, v3, v2
	v_mul_f32_e32 v128, v3, v128
	v_mul_f32_e32 v2, v2, v18
	v_mul_f32_e32 v128, v128, v19
	v_mov_b32_e32 v151, 0
	v_cvt_pk_fp8_f32 v151, v2, v128
	v_lshlrev_b32_e32 v150, 16, v129
	v_and_b32_e32 v2, 0xffff0000, v129
	v_mul_f32_e32 v150, v3, v150
	v_mul_f32_e32 v2, v3, v2
	v_mul_f32_e32 v150, v150, v20
	v_mul_f32_e32 v2, v2, v21
	v_cvt_pk_fp8_f32 v151, v150, v2 op_sel:[0,0,1]
	v_lshlrev_b32_e32 v2, 16, v126
	v_and_b32_e32 v126, 0xffff0000, v126
	v_mul_f32_e32 v2, v3, v2
	v_mul_f32_e32 v126, v3, v126
	v_mul_f32_e32 v2, v2, v14
	v_mul_f32_e32 v126, v126, v15
	v_mov_b32_e32 v129, 0
	v_cvt_pk_fp8_f32 v129, v2, v126
	v_lshlrev_b32_e32 v128, 16, v127
	v_and_b32_e32 v2, 0xffff0000, v127
	v_mul_f32_e32 v128, v3, v128
	v_mul_f32_e32 v2, v3, v2
	v_mul_f32_e32 v128, v128, v16
	v_mul_f32_e32 v2, v2, v17
	v_cvt_pk_fp8_f32 v129, v128, v2 op_sel:[0,0,1]
	v_lshlrev_b32_e32 v2, 16, v124
	v_and_b32_e32 v124, 0xffff0000, v124
	v_mul_f32_e32 v2, v3, v2
	v_mul_f32_e32 v124, v3, v124
	v_mul_f32_e32 v2, v2, v10
	v_mul_f32_e32 v124, v124, v11
	v_mov_b32_e32 v127, 0
	v_cvt_pk_fp8_f32 v127, v2, v124
	v_lshlrev_b32_e32 v126, 16, v125
	v_and_b32_e32 v2, 0xffff0000, v125
	v_mul_f32_e32 v126, v3, v126
	v_mul_f32_e32 v2, v3, v2
	v_mul_f32_e32 v126, v126, v12
	v_mul_f32_e32 v2, v2, v13
	v_cvt_pk_fp8_f32 v127, v126, v2 op_sel:[0,0,1]
	v_lshlrev_b32_e32 v2, 16, v122
	v_and_b32_e32 v122, 0xffff0000, v122
	v_mul_f32_e32 v2, v3, v2
	v_mul_f32_e32 v122, v3, v122
	v_mul_f32_e32 v2, v2, v6
	v_mul_f32_e32 v122, v122, v7
	v_mov_b32_e32 v125, 0
	v_cvt_pk_fp8_f32 v125, v2, v122
	v_lshlrev_b32_e32 v124, 16, v123
	v_and_b32_e32 v2, 0xffff0000, v123
	v_mul_f32_e32 v124, v3, v124
	v_mul_f32_e32 v2, v3, v2
	v_mul_f32_e32 v124, v124, v8
	v_mul_f32_e32 v2, v2, v9
	v_cvt_pk_fp8_f32 v125, v124, v2 op_sel:[0,0,1]
	v_lshlrev_b32_e32 v2, 16, v120
	v_and_b32_e32 v3, 0xffff0000, v120
	v_mul_f32_e32 v2, v4, v2
	v_mul_f32_e32 v3, v4, v3
	v_mul_f32_e32 v2, v2, v34
	v_mul_f32_e32 v3, v3, v35
	v_mov_b32_e32 v122, 0
	v_cvt_pk_fp8_f32 v122, v2, v3
	v_lshlrev_b32_e32 v120, 16, v121
	v_and_b32_e32 v2, 0xffff0000, v121
	v_mul_f32_e32 v120, v4, v120
	v_mul_f32_e32 v2, v4, v2
	v_mul_f32_e32 v120, v120, v36
	v_mul_f32_e32 v2, v2, v37
	v_cvt_pk_fp8_f32 v122, v120, v2 op_sel:[0,0,1]
	v_lshlrev_b32_e32 v2, 16, v118
	v_and_b32_e32 v3, 0xffff0000, v118
	v_mul_f32_e32 v2, v4, v2
	v_mul_f32_e32 v3, v4, v3
	v_mul_f32_e32 v2, v2, v30
	v_mul_f32_e32 v3, v3, v31
	v_mov_b32_e32 v120, 0
	v_cvt_pk_fp8_f32 v120, v2, v3
	v_lshlrev_b32_e32 v118, 16, v119
	v_and_b32_e32 v2, 0xffff0000, v119
	v_mul_f32_e32 v118, v4, v118
	v_mul_f32_e32 v2, v4, v2
	v_mul_f32_e32 v118, v118, v32
	v_mul_f32_e32 v2, v2, v33
	v_cvt_pk_fp8_f32 v120, v118, v2 op_sel:[0,0,1]
	v_lshlrev_b32_e32 v2, 16, v116
	v_and_b32_e32 v3, 0xffff0000, v116
	v_mul_f32_e32 v2, v4, v2
	v_mul_f32_e32 v3, v4, v3
	v_mul_f32_e32 v2, v2, v26
	v_mul_f32_e32 v3, v3, v27
	v_mov_b32_e32 v118, 0
	v_cvt_pk_fp8_f32 v118, v2, v3
	v_lshlrev_b32_e32 v116, 16, v117
	v_and_b32_e32 v2, 0xffff0000, v117
	v_mul_f32_e32 v116, v4, v116
	v_mul_f32_e32 v2, v4, v2
	v_mul_f32_e32 v116, v116, v28
	v_mul_f32_e32 v2, v2, v29
	v_cvt_pk_fp8_f32 v118, v116, v2 op_sel:[0,0,1]
	v_lshlrev_b32_e32 v2, 16, v114
	v_and_b32_e32 v3, 0xffff0000, v114
	v_mul_f32_e32 v2, v4, v2
	v_mul_f32_e32 v3, v4, v3
	v_mul_f32_e32 v2, v2, v22
	v_mul_f32_e32 v3, v3, v23
	v_mov_b32_e32 v116, 0
	v_cvt_pk_fp8_f32 v116, v2, v3
	v_lshlrev_b32_e32 v114, 16, v115
	v_and_b32_e32 v2, 0xffff0000, v115
	v_mul_f32_e32 v114, v4, v114
	v_mul_f32_e32 v2, v4, v2
	v_mul_f32_e32 v114, v114, v24
	v_mul_f32_e32 v2, v2, v25
	v_cvt_pk_fp8_f32 v116, v114, v2 op_sel:[0,0,1]
	v_lshlrev_b32_e32 v2, 16, v112
	v_and_b32_e32 v3, 0xffff0000, v112
	v_mul_f32_e32 v2, v4, v2
	v_mul_f32_e32 v3, v4, v3
	v_mul_f32_e32 v2, v2, v18
	v_mul_f32_e32 v3, v3, v19
	v_mov_b32_e32 v114, 0
	v_cvt_pk_fp8_f32 v114, v2, v3
	v_lshlrev_b32_e32 v112, 16, v113
	v_and_b32_e32 v2, 0xffff0000, v113
	v_mul_f32_e32 v112, v4, v112
	v_mul_f32_e32 v2, v4, v2
	v_mul_f32_e32 v112, v112, v20
	v_mul_f32_e32 v2, v2, v21
	v_cvt_pk_fp8_f32 v114, v112, v2 op_sel:[0,0,1]
	v_lshlrev_b32_e32 v2, 16, v110
	v_and_b32_e32 v3, 0xffff0000, v110
	v_mul_f32_e32 v2, v4, v2
	v_mul_f32_e32 v3, v4, v3
	v_mul_f32_e32 v2, v2, v14
	v_mul_f32_e32 v3, v3, v15
	v_mov_b32_e32 v112, 0
	v_cvt_pk_fp8_f32 v112, v2, v3
	v_lshlrev_b32_e32 v110, 16, v111
	v_and_b32_e32 v2, 0xffff0000, v111
	v_mul_f32_e32 v110, v4, v110
	v_mul_f32_e32 v2, v4, v2
	v_mul_f32_e32 v110, v110, v16
	v_mul_f32_e32 v2, v2, v17
	v_cvt_pk_fp8_f32 v112, v110, v2 op_sel:[0,0,1]
	v_lshlrev_b32_e32 v2, 16, v108
	v_and_b32_e32 v3, 0xffff0000, v108
	v_mul_f32_e32 v2, v4, v2
	v_mul_f32_e32 v3, v4, v3
	v_mul_f32_e32 v2, v2, v10
	v_mul_f32_e32 v3, v3, v11
	v_mov_b32_e32 v110, 0
	v_cvt_pk_fp8_f32 v110, v2, v3
	v_lshlrev_b32_e32 v108, 16, v109
	v_and_b32_e32 v2, 0xffff0000, v109
	v_mul_f32_e32 v108, v4, v108
	v_mul_f32_e32 v2, v4, v2
	v_mul_f32_e32 v108, v108, v12
	v_mul_f32_e32 v2, v2, v13
	v_cvt_pk_fp8_f32 v110, v108, v2 op_sel:[0,0,1]
	v_lshlrev_b32_e32 v2, 16, v106
	v_and_b32_e32 v3, 0xffff0000, v106
	v_mul_f32_e32 v2, v4, v2
	v_mul_f32_e32 v3, v4, v3
	v_mul_f32_e32 v2, v2, v6
	v_mul_f32_e32 v3, v3, v7
	v_mov_b32_e32 v108, 0
	v_cvt_pk_fp8_f32 v108, v2, v3
	v_lshlrev_b32_e32 v106, 16, v107
	v_and_b32_e32 v2, 0xffff0000, v107
	v_mul_f32_e32 v106, v4, v106
	v_mul_f32_e32 v2, v4, v2
	v_mul_f32_e32 v106, v106, v8
	v_mul_f32_e32 v2, v2, v9
	v_cvt_pk_fp8_f32 v108, v106, v2 op_sel:[0,0,1]
	v_lshlrev_b32_e32 v2, 16, v104
	v_and_b32_e32 v3, 0xffff0000, v104
	v_mul_f32_e32 v2, v5, v2
	v_mul_f32_e32 v3, v5, v3
	v_mul_f32_e32 v2, v2, v34
	v_mul_f32_e32 v3, v3, v35
	v_mov_b32_e32 v34, 0
	v_cvt_pk_fp8_f32 v34, v2, v3
	v_lshlrev_b32_e32 v4, 16, v105
	v_and_b32_e32 v2, 0xffff0000, v105
	v_mul_f32_e32 v4, v5, v4
	v_mul_f32_e32 v2, v5, v2
	v_mul_f32_e32 v4, v4, v36
	v_mul_f32_e32 v2, v2, v37
	v_cvt_pk_fp8_f32 v34, v4, v2 op_sel:[0,0,1]
	v_lshlrev_b32_e32 v2, 16, v102
	v_and_b32_e32 v3, 0xffff0000, v102
	v_mul_f32_e32 v2, v5, v2
	v_mul_f32_e32 v3, v5, v3
	v_mul_f32_e32 v2, v2, v30
	v_mul_f32_e32 v3, v3, v31
	v_mov_b32_e32 v30, 0
	v_cvt_pk_fp8_f32 v30, v2, v3
	v_lshlrev_b32_e32 v4, 16, v103
	v_and_b32_e32 v2, 0xffff0000, v103
	v_mul_f32_e32 v4, v5, v4
	v_mul_f32_e32 v2, v5, v2
	v_mul_f32_e32 v4, v4, v32
	v_mul_f32_e32 v2, v2, v33
	v_cvt_pk_fp8_f32 v30, v4, v2 op_sel:[0,0,1]
	v_lshlrev_b32_e32 v2, 16, v100
	v_and_b32_e32 v3, 0xffff0000, v100
	v_mul_f32_e32 v2, v5, v2
	v_mul_f32_e32 v3, v5, v3
	v_mul_f32_e32 v2, v2, v26
	v_mul_f32_e32 v3, v3, v27
	v_mov_b32_e32 v26, 0
	v_cvt_pk_fp8_f32 v26, v2, v3
	v_lshlrev_b32_e32 v4, 16, v101
	v_and_b32_e32 v2, 0xffff0000, v101
	v_mul_f32_e32 v4, v5, v4
	v_mul_f32_e32 v2, v5, v2
	v_mul_f32_e32 v4, v4, v28
	v_mul_f32_e32 v2, v2, v29
	v_cvt_pk_fp8_f32 v26, v4, v2 op_sel:[0,0,1]
	v_lshlrev_b32_e32 v2, 16, v98
	v_and_b32_e32 v3, 0xffff0000, v98
	v_mul_f32_e32 v2, v5, v2
	v_mul_f32_e32 v3, v5, v3
	v_mul_f32_e32 v2, v2, v22
	v_mul_f32_e32 v3, v3, v23
	v_mov_b32_e32 v22, 0
	v_cvt_pk_fp8_f32 v22, v2, v3
	v_lshlrev_b32_e32 v4, 16, v99
	v_and_b32_e32 v2, 0xffff0000, v99
	v_mul_f32_e32 v4, v5, v4
	v_mul_f32_e32 v2, v5, v2
	v_mul_f32_e32 v4, v4, v24
	v_mul_f32_e32 v2, v2, v25
	v_cvt_pk_fp8_f32 v22, v4, v2 op_sel:[0,0,1]
	v_lshlrev_b32_e32 v2, 16, v96
	v_and_b32_e32 v3, 0xffff0000, v96
	v_mul_f32_e32 v2, v5, v2
	v_mul_f32_e32 v3, v5, v3
	v_mul_f32_e32 v2, v2, v18
	v_mul_f32_e32 v3, v3, v19
	v_mov_b32_e32 v18, 0
	v_cvt_pk_fp8_f32 v18, v2, v3
	v_lshlrev_b32_e32 v4, 16, v97
	v_and_b32_e32 v2, 0xffff0000, v97
	v_mul_f32_e32 v4, v5, v4
	v_mul_f32_e32 v2, v5, v2
	v_mul_f32_e32 v4, v4, v20
	v_mul_f32_e32 v2, v2, v21
	v_cvt_pk_fp8_f32 v18, v4, v2 op_sel:[0,0,1]
	v_lshlrev_b32_e32 v2, 16, v94
	v_and_b32_e32 v3, 0xffff0000, v94
	v_mul_f32_e32 v2, v5, v2
	v_mul_f32_e32 v3, v5, v3
	v_mul_f32_e32 v2, v2, v14
	v_mul_f32_e32 v3, v3, v15
	v_mov_b32_e32 v14, 0
	v_cvt_pk_fp8_f32 v14, v2, v3
	v_lshlrev_b32_e32 v4, 16, v95
	v_and_b32_e32 v2, 0xffff0000, v95
	v_mul_f32_e32 v4, v5, v4
	v_mul_f32_e32 v2, v5, v2
	v_mul_f32_e32 v4, v4, v16
	v_mul_f32_e32 v2, v2, v17
	v_cvt_pk_fp8_f32 v14, v4, v2 op_sel:[0,0,1]
	v_lshlrev_b32_e32 v2, 16, v92
	v_and_b32_e32 v3, 0xffff0000, v92
	v_mul_f32_e32 v2, v5, v2
	v_mul_f32_e32 v3, v5, v3
	v_mul_f32_e32 v2, v2, v10
	v_mul_f32_e32 v3, v3, v11
	v_mov_b32_e32 v10, 0
	v_cvt_pk_fp8_f32 v10, v2, v3
	v_lshlrev_b32_e32 v4, 16, v93
	v_and_b32_e32 v2, 0xffff0000, v93
	v_mul_f32_e32 v4, v5, v4
	v_mul_f32_e32 v2, v5, v2
	v_mul_f32_e32 v4, v4, v12
	v_mul_f32_e32 v2, v2, v13
	v_cvt_pk_fp8_f32 v10, v4, v2 op_sel:[0,0,1]
	v_lshlrev_b32_e32 v2, 16, v90
	v_and_b32_e32 v3, 0xffff0000, v90
	v_mul_f32_e32 v2, v5, v2
	v_mul_f32_e32 v3, v5, v3
	v_mul_f32_e32 v2, v2, v6
	v_mul_f32_e32 v3, v3, v7
	v_mov_b32_e32 v6, 0
	v_cvt_pk_fp8_f32 v6, v2, v3
	v_lshlrev_b32_e32 v4, 16, v91
	v_and_b32_e32 v2, 0xffff0000, v91
	v_mul_f32_e32 v4, v5, v4
	v_mul_f32_e32 v2, v5, v2
	v_mul_f32_e32 v4, v4, v8
	v_mul_f32_e32 v2, v2, v9
	v_cvt_pk_fp8_f32 v6, v4, v2 op_sel:[0,0,1]
	ds_write2st64_b32 v130, v152, v153 offset0:72 offset1:73
	ds_write2st64_b32 v130, v154, v155 offset0:74 offset1:75
	ds_write2st64_b32 v130, v151, v129 offset0:76 offset1:77
	ds_write2st64_b32 v130, v127, v125 offset0:78 offset1:79
	ds_write2st64_b32 v130, v122, v120 offset0:80 offset1:81
	ds_write2st64_b32 v130, v118, v116 offset0:82 offset1:83
	ds_write2st64_b32 v130, v114, v112 offset0:84 offset1:85
	ds_write2st64_b32 v130, v110, v108 offset0:86 offset1:87
	ds_write2st64_b32 v130, v34, v30 offset0:88 offset1:89
	ds_write2st64_b32 v130, v26, v22 offset0:90 offset1:91
	ds_write2st64_b32 v130, v18, v14 offset0:92 offset1:93
	ds_write2st64_b32 v130, v10, v6 offset0:94 offset1:95
	s_waitcnt lgkmcnt(0)
	v_add_u32_e32 v12, s38, v38
	ds_read_b128 v[2:5], v12 offset:16384
	ds_read_b128 v[6:9], v12 offset:17408
	v_lshl_add_u64 v[10:11], v[52:53], 0, s[12:13]
	s_lshl_b64 s[12:13], s[28:29], 11
	s_waitcnt lgkmcnt(1)
	global_store_dwordx4 v[10:11], v[2:5], off
	ds_read_b128 v[2:5], v12 offset:18432
	s_waitcnt lgkmcnt(1)
	global_store_dwordx4 v[10:11], v[6:9], off offset:1024
	v_lshl_add_u64 v[10:11], v[52:53], 0, s[12:13]
	ds_read_b128 v[6:9], v12 offset:19456
	s_lshl_b64 s[12:13], s[26:27], 11
	s_waitcnt lgkmcnt(1)
	global_store_dwordx4 v[10:11], v[2:5], off
	ds_read_b128 v[2:5], v12 offset:20480
	v_lshl_add_u64 v[14:15], v[52:53], 0, s[12:13]
	s_waitcnt lgkmcnt(1)
	global_store_dwordx4 v[10:11], v[6:9], off offset:1024
	ds_read_b128 v[6:9], v12 offset:21504
	s_lshl_b64 s[12:13], s[24:25], 11
	s_waitcnt lgkmcnt(1)
	global_store_dwordx4 v[14:15], v[2:5], off
	ds_read_b128 v[2:5], v12 offset:22528
	ds_read_b128 v[10:13], v12 offset:23552
	s_waitcnt lgkmcnt(2)
	global_store_dwordx4 v[14:15], v[6:9], off offset:1024
	s_nop 1
	v_lshl_add_u64 v[6:7], v[52:53], 0, s[12:13]
	s_waitcnt lgkmcnt(1)
	global_store_dwordx4 v[6:7], v[2:5], off
	s_waitcnt lgkmcnt(0)
	global_store_dwordx4 v[6:7], v[10:13], off offset:1024
	v_cmp_gt_i32_e64 s[12:13], s39, v131
	s_nop 0
	s_nop 0
	v_cndmask_b32_e64 v18, 0, v198, s[12:13]
	v_cmp_gt_i32_e64 s[12:13], s39, v132
	s_nop 0
	v_add_u32_e32 v2, v199, v198
	s_nop 0
	v_add3_u32 v2, v2, v200, v201
	v_cndmask_b32_e64 v3, 0, v199, s[12:13]
	v_cmp_gt_i32_e64 s[12:13], s39, v133
	v_add_u32_e32 v3, v3, v18
	s_nop 0
	v_add3_u32 v2, v2, v202, v203
	v_cndmask_b32_e64 v18, 0, v200, s[12:13]
	v_cmp_gt_i32_e64 s[12:13], s39, v134
	s_nop 0
	v_add3_u32 v2, v2, v204, v205
	s_nop 0
	v_add3_u32 v2, v2, v206, v207
	v_cndmask_b32_e64 v4, 0, v201, s[12:13]
	v_cmp_gt_i32_e64 s[12:13], s39, v135
	v_add3_u32 v3, v3, v18, v4
	s_nop 0
	v_add3_u32 v2, v2, v208, v209
	v_cndmask_b32_e64 v4, 0, v202, s[12:13]
	v_cmp_gt_i32_e64 s[12:13], s39, v136
	s_nop 0
	v_add3_u32 v2, v2, v210, v211
	s_nop 0
	v_add3_u32 v2, v2, v212, v213
	v_cndmask_b32_e64 v5, 0, v203, s[12:13]
	v_cmp_gt_i32_e64 s[12:13], s39, v137
	v_add3_u32 v3, v3, v4, v5
	s_nop 0
	v_cndmask_b32_e64 v4, 0, v204, s[12:13]
	v_cmp_gt_i32_e64 s[12:13], s39, v138
	s_nop 1
	v_cndmask_b32_e64 v5, 0, v205, s[12:13]
	v_cmp_gt_i32_e64 s[12:13], s39, v139
	v_add3_u32 v3, v3, v4, v5
	s_nop 0
	v_cndmask_b32_e64 v4, 0, v206, s[12:13]
	v_cmp_gt_i32_e64 s[12:13], s39, v140
	s_nop 1
	v_cndmask_b32_e64 v5, 0, v207, s[12:13]
	v_cmp_gt_i32_e64 s[12:13], s39, v141
	v_add3_u32 v3, v3, v4, v5
	s_nop 0
	v_cndmask_b32_e64 v4, 0, v208, s[12:13]
	v_cmp_gt_i32_e64 s[12:13], s39, v142
	s_nop 1
	v_cndmask_b32_e64 v5, 0, v209, s[12:13]
	v_cmp_gt_i32_e64 s[12:13], s39, v143
	v_add3_u32 v3, v3, v4, v5
	s_nop 0
	v_cndmask_b32_e64 v4, 0, v210, s[12:13]
	v_cmp_gt_i32_e64 s[12:13], s39, v144
	s_nop 1
	v_cndmask_b32_e64 v5, 0, v211, s[12:13]
	v_cmp_gt_i32_e64 s[12:13], s39, v145
	v_add3_u32 v3, v3, v4, v5
	s_nop 0
	v_cndmask_b32_e64 v4, 0, v212, s[12:13]
	v_cmp_gt_i32_e64 s[12:13], s39, v146
	s_nop 1
	v_cndmask_b32_e64 v5, 0, v213, s[12:13]
	v_add3_u32 v3, v3, v4, v5
	ds_write2st64_b32 v147, v2, v3 offset1:8
	v_lshl_or_b32 v2, s39, 7, v0
	s_and_saveexec_b64 s[12:13], vcc
	s_cbranch_execz .LBB0_1155
	ds_write_b32 v147, v216 offset:4224
